# v83 + gate/up token-table set-up: all units' LDS lookups issued together, then all list loads, then the stores (was one unit at a time)
# baseline (speedup 1.0000x reference)
; #define LAS __attribute__((address_space(3)))
;     __device__ __forceinline__ bool next(int i, pg8::Unit& u) const { const int L = i * G + c; if (L >= 256) return false; u.pm = L >> 1; u.pn = L & 1; u.ord = i; return true; }
;     __device__ __forceinline__ int vcu() const { return (G % 8 == 0) ? (c % 8) * (G / 8) + c / 8 : c; }
;     __device__ __forceinline__ int vcu() const { return (G % 8 == 0) ? (c % 8) * (G / 8) + c / 8 : c; }
;     __device__ __forceinline__ bool next(int i, pg8::Unit& u) const { const int L = i * G + c; if (L >= 64) return false; u.pm = L >> 1; u.pn = L & 1; u.ord = i; return true; }
;     __device__ __forceinline__ bool next(int i, pg8::Unit& u) const {
;         const int L = i * G + vcu(); if (L >= nunits || i >= MOE_MAX_ORD) return false;
;         const int q = L >> 1; const int e = __builtin_amdgcn_readfirstlane((q < R) ? (int)((LAS unsigned short*)(lds + MOE_TAB_OFF + 2176))[q] : 256);
;         u.pm = q; u.pn = e * 2 + (L & 1); u.ord = i; return true; }
;     __device__ __forceinline__ void prepare() const {
;         const int tid = threadIdx.x, r = tid & 255;
;         pg8::Unit u;
;         for (int i = tid >> 8; next(i, u); i += 2) {
;             const int e = u.pn >> 1; int token;
;             if (e < 256) { const int ts = ((LAS int*)(lds + MOE_TAB_OFF))[e], cn = ((LAS int*)(lds + MOE_TAB_OFF + 1088))[e]; int lr = (u.pm - ts) * 256 + r; if (lr >= cn) lr = cn - 1;
;                 token = list[(size_t)e * LISTCAP + lr].x / 10; }
;             else token = (u.pm - R) * 256 + r;
;             ((LAS unsigned short*)(lds + MOE_TOK_OFF))[i * 256 + r] = (unsigned short)token;
;         }
.LBB0_727:
	s_or_b64 exec, exec, s[0:1]
	s_add_i32 s0, 0, 0x20400
	v_mov_b32_e32 v1, s0
	s_waitcnt lgkmcnt(0)
	s_barrier
	ds_read_b32 v1, v1
	s_load_dwordx2 s[4:5], s[82:83], 0xf0
	s_load_dword s13, s[82:83], 0x120
	s_waitcnt lgkmcnt(0)
	v_readfirstlane_b32 s15, v1
	s_lshl_b32 s28, s15, 1
	s_addk_i32 s28, 0x100
	s_add_u32 s2, s82, 0x120
	s_addc_u32 s3, s83, 0
	s_ashr_i32 s6, s33, 31
	s_lshr_b32 s6, s6, 29
	s_add_i32 s6, s33, s6
	s_ashr_i32 s7, s6, 3
	s_and_b32 s6, s6, -8
	s_ashr_i32 s1, s13, 3
	s_sub_i32 s6, s33, s6
	s_mul_i32 s1, s1, s6
	s_and_b32 s0, s13, 7
	s_add_i32 s1, s1, s7
	v_lshrrev_b32_e32 v1, 8, v0
	s_cmp_eq_u32 s0, 0
	s_cselect_b32 s29, s1, s33
	v_mul_lo_u32 v2, v1, s13
	v_add_u32_e32 v3, s29, v2
	v_cmp_gt_i32_e32 vcc, s28, v3
	s_and_saveexec_b64 s[6:7], vcc
	s_cbranch_execz .LBB0_736
	v_and_b32_e32 v3, 0xff, v0
	v_lshlrev_b32_e32 v5, 1, v3
	v_lshl_or_b32 v5, v1, 9, v5
	v_add_u32_e32 v5, 0x21400, v5
	v_mov_b32_e32 v9, 0
	s_add_u32 s8, s4, 0xa100000
	s_addc_u32 s9, s5, 0
	s_mov_b32 s17, 0x66666667
	v_readfirstlane_b32 s0, v1
	s_mul_i32 s1, s0, s13
	s_add_i32 s18, s29, s1
	s_lshl_b32 s16, s13, 1
	s_mov_b32 s10, 0
	s_mov_b32 s11, s18
.Lprep_cnt_l0:
	s_add_i32 s10, s10, 1
	s_add_i32 s11, s11, s16
	s_cmp_ge_i32 s11, s28
	s_cbranch_scc1 .Lprep_cnt_done_l0
	s_cmp_lt_u32 s10, 10
	s_cbranch_scc1 .Lprep_cnt_l0
.Lprep_cnt_done_l0:
	s_mov_b32 s11, s18
	s_cmp_le_u32 s10, 0
	s_cbranch_scc1 .Lprep_a1e_l0
	s_ashr_i32 s0, s11, 1
	v_mov_b32_e32 v20, 0x100
	s_cmp_ge_i32 s0, s15
	s_cbranch_scc1 .Lprep_a1s_l0_0
	s_lshl_b32 s1, s0, 1
	s_add_i32 s1, s1, 0x20880
	v_mov_b32_e32 v6, s1
	ds_read_u16 v20, v6
.Lprep_a1s_l0_0:
	s_add_i32 s11, s11, s16
	s_cmp_le_u32 s10, 1
	s_cbranch_scc1 .Lprep_a1e_l0
	s_ashr_i32 s0, s11, 1
	v_mov_b32_e32 v21, 0x100
	s_cmp_ge_i32 s0, s15
	s_cbranch_scc1 .Lprep_a1s_l0_1
	s_lshl_b32 s1, s0, 1
	s_add_i32 s1, s1, 0x20880
	v_mov_b32_e32 v6, s1
	ds_read_u16 v21, v6
.Lprep_a1s_l0_1:
	s_add_i32 s11, s11, s16
	s_cmp_le_u32 s10, 2
	s_cbranch_scc1 .Lprep_a1e_l0
	s_ashr_i32 s0, s11, 1
	v_mov_b32_e32 v22, 0x100
	s_cmp_ge_i32 s0, s15
	s_cbranch_scc1 .Lprep_a1s_l0_2
	s_lshl_b32 s1, s0, 1
	s_add_i32 s1, s1, 0x20880
	v_mov_b32_e32 v6, s1
	ds_read_u16 v22, v6
.Lprep_a1s_l0_2:
	s_add_i32 s11, s11, s16
	s_cmp_le_u32 s10, 3
	s_cbranch_scc1 .Lprep_a1e_l0
	s_ashr_i32 s0, s11, 1
	v_mov_b32_e32 v23, 0x100
	s_cmp_ge_i32 s0, s15
	s_cbranch_scc1 .Lprep_a1s_l0_3
	s_lshl_b32 s1, s0, 1
	s_add_i32 s1, s1, 0x20880
	v_mov_b32_e32 v6, s1
	ds_read_u16 v23, v6
.Lprep_a1s_l0_3:
	s_add_i32 s11, s11, s16
	s_cmp_le_u32 s10, 4
	s_cbranch_scc1 .Lprep_a1e_l0
	s_ashr_i32 s0, s11, 1
	v_mov_b32_e32 v24, 0x100
	s_cmp_ge_i32 s0, s15
	s_cbranch_scc1 .Lprep_a1s_l0_4
	s_lshl_b32 s1, s0, 1
	s_add_i32 s1, s1, 0x20880
	v_mov_b32_e32 v6, s1
	ds_read_u16 v24, v6
.Lprep_a1s_l0_4:
	s_add_i32 s11, s11, s16
	s_cmp_le_u32 s10, 5
	s_cbranch_scc1 .Lprep_a1e_l0
	s_ashr_i32 s0, s11, 1
	v_mov_b32_e32 v25, 0x100
	s_cmp_ge_i32 s0, s15
	s_cbranch_scc1 .Lprep_a1s_l0_5
	s_lshl_b32 s1, s0, 1
	s_add_i32 s1, s1, 0x20880
	v_mov_b32_e32 v6, s1
	ds_read_u16 v25, v6
.Lprep_a1s_l0_5:
	s_add_i32 s11, s11, s16
	s_cmp_le_u32 s10, 6
	s_cbranch_scc1 .Lprep_a1e_l0
	s_ashr_i32 s0, s11, 1
	v_mov_b32_e32 v26, 0x100
	s_cmp_ge_i32 s0, s15
	s_cbranch_scc1 .Lprep_a1s_l0_6
	s_lshl_b32 s1, s0, 1
	s_add_i32 s1, s1, 0x20880
	v_mov_b32_e32 v6, s1
	ds_read_u16 v26, v6
.Lprep_a1s_l0_6:
	s_add_i32 s11, s11, s16
	s_cmp_le_u32 s10, 7
	s_cbranch_scc1 .Lprep_a1e_l0
	s_ashr_i32 s0, s11, 1
	v_mov_b32_e32 v27, 0x100
	s_cmp_ge_i32 s0, s15
	s_cbranch_scc1 .Lprep_a1s_l0_7
	s_lshl_b32 s1, s0, 1
	s_add_i32 s1, s1, 0x20880
	v_mov_b32_e32 v6, s1
	ds_read_u16 v27, v6
.Lprep_a1s_l0_7:
	s_add_i32 s11, s11, s16
	s_cmp_le_u32 s10, 8
	s_cbranch_scc1 .Lprep_a1e_l0
	s_ashr_i32 s0, s11, 1
	v_mov_b32_e32 v28, 0x100
	s_cmp_ge_i32 s0, s15
	s_cbranch_scc1 .Lprep_a1s_l0_8
	s_lshl_b32 s1, s0, 1
	s_add_i32 s1, s1, 0x20880
	v_mov_b32_e32 v6, s1
	ds_read_u16 v28, v6
.Lprep_a1s_l0_8:
	s_add_i32 s11, s11, s16
	s_cmp_le_u32 s10, 9
	s_cbranch_scc1 .Lprep_a1e_l0
	s_ashr_i32 s0, s11, 1
	v_mov_b32_e32 v29, 0x100
	s_cmp_ge_i32 s0, s15
	s_cbranch_scc1 .Lprep_a1s_l0_9
	s_lshl_b32 s1, s0, 1
	s_add_i32 s1, s1, 0x20880
	v_mov_b32_e32 v6, s1
	ds_read_u16 v29, v6
.Lprep_a1s_l0_9:
	s_add_i32 s11, s11, s16
.Lprep_a1e_l0:
	s_waitcnt lgkmcnt(0)
	s_cmp_le_u32 s10, 0
	s_cbranch_scc1 .Lprep_a2e_l0
	v_min_u32_e32 v6, 0xff, v20
	v_lshlrev_b32_e32 v6, 2, v6
	v_add_u32_e32 v6, 0x20000, v6
	ds_read_b32 v30, v6
	ds_read_b32 v40, v6 offset:1088
	s_cmp_le_u32 s10, 1
	s_cbranch_scc1 .Lprep_a2e_l0
	v_min_u32_e32 v6, 0xff, v21
	v_lshlrev_b32_e32 v6, 2, v6
	v_add_u32_e32 v6, 0x20000, v6
	ds_read_b32 v31, v6
	ds_read_b32 v41, v6 offset:1088
	s_cmp_le_u32 s10, 2
	s_cbranch_scc1 .Lprep_a2e_l0
	v_min_u32_e32 v6, 0xff, v22
	v_lshlrev_b32_e32 v6, 2, v6
	v_add_u32_e32 v6, 0x20000, v6
	ds_read_b32 v32, v6
	ds_read_b32 v42, v6 offset:1088
	s_cmp_le_u32 s10, 3
	s_cbranch_scc1 .Lprep_a2e_l0
	v_min_u32_e32 v6, 0xff, v23
	v_lshlrev_b32_e32 v6, 2, v6
	v_add_u32_e32 v6, 0x20000, v6
	ds_read_b32 v33, v6
	ds_read_b32 v43, v6 offset:1088
	s_cmp_le_u32 s10, 4
	s_cbranch_scc1 .Lprep_a2e_l0
	v_min_u32_e32 v6, 0xff, v24
	v_lshlrev_b32_e32 v6, 2, v6
	v_add_u32_e32 v6, 0x20000, v6
	ds_read_b32 v34, v6
	ds_read_b32 v44, v6 offset:1088
	s_cmp_le_u32 s10, 5
	s_cbranch_scc1 .Lprep_a2e_l0
	v_min_u32_e32 v6, 0xff, v25
	v_lshlrev_b32_e32 v6, 2, v6
	v_add_u32_e32 v6, 0x20000, v6
	ds_read_b32 v35, v6
	ds_read_b32 v45, v6 offset:1088
	s_cmp_le_u32 s10, 6
	s_cbranch_scc1 .Lprep_a2e_l0
	v_min_u32_e32 v6, 0xff, v26
	v_lshlrev_b32_e32 v6, 2, v6
	v_add_u32_e32 v6, 0x20000, v6
	ds_read_b32 v36, v6
	ds_read_b32 v46, v6 offset:1088
	s_cmp_le_u32 s10, 7
	s_cbranch_scc1 .Lprep_a2e_l0
	v_min_u32_e32 v6, 0xff, v27
	v_lshlrev_b32_e32 v6, 2, v6
	v_add_u32_e32 v6, 0x20000, v6
	ds_read_b32 v37, v6
	ds_read_b32 v47, v6 offset:1088
	s_cmp_le_u32 s10, 8
	s_cbranch_scc1 .Lprep_a2e_l0
	v_min_u32_e32 v6, 0xff, v28
	v_lshlrev_b32_e32 v6, 2, v6
	v_add_u32_e32 v6, 0x20000, v6
	ds_read_b32 v38, v6
	ds_read_b32 v48, v6 offset:1088
	s_cmp_le_u32 s10, 9
	s_cbranch_scc1 .Lprep_a2e_l0
	v_min_u32_e32 v6, 0xff, v29
	v_lshlrev_b32_e32 v6, 2, v6
	v_add_u32_e32 v6, 0x20000, v6
	ds_read_b32 v39, v6
	ds_read_b32 v49, v6 offset:1088
; #define LAS __attribute__((address_space(3)))
;     __device__ __forceinline__ void prepare() const {
;     ...
;             if (e < 256) { const int ts = ((LAS int*)(lds + MOE_TAB_OFF))[e], cn = ((LAS int*)(lds + MOE_TAB_OFF + 1088))[e]; int lr = (u.pm - ts) * 256 + r; if (lr >= cn) lr = cn - 1;
;                 token = list[(size_t)e * LISTCAP + lr].x / 10; }
.Lprep_a2e_l0:
	s_waitcnt lgkmcnt(0)
	s_mov_b32 s11, s18
	s_cmp_le_u32 s10, 0
	s_cbranch_scc1 .Lprep_a3e_l0
	s_ashr_i32 s0, s11, 1
	v_sub_u32_e32 v6, s0, v30
	v_lshl_or_b32 v6, v6, 8, v3
	v_add_u32_e32 v7, -1, v40
	v_min_i32_e32 v6, v6, v7
	v_ashrrev_i32_e32 v7, 31, v6
	v_min_u32_e32 v8, 0xff, v20
	v_lshlrev_b32_e32 v8, 18, v8
	v_lshl_add_u64 v[6:7], v[6:7], 3, s[8:9]
	v_lshl_add_u64 v[6:7], v[6:7], 0, v[8:9]
	global_load_dword v50, v[6:7], off
	s_add_i32 s11, s11, s16
	s_cmp_le_u32 s10, 1
	s_cbranch_scc1 .Lprep_a3e_l0
	s_ashr_i32 s0, s11, 1
	v_sub_u32_e32 v6, s0, v31
	v_lshl_or_b32 v6, v6, 8, v3
	v_add_u32_e32 v7, -1, v41
	v_min_i32_e32 v6, v6, v7
	v_ashrrev_i32_e32 v7, 31, v6
	v_min_u32_e32 v8, 0xff, v21
	v_lshlrev_b32_e32 v8, 18, v8
	v_lshl_add_u64 v[6:7], v[6:7], 3, s[8:9]
	v_lshl_add_u64 v[6:7], v[6:7], 0, v[8:9]
	global_load_dword v51, v[6:7], off
	s_add_i32 s11, s11, s16
	s_cmp_le_u32 s10, 2
	s_cbranch_scc1 .Lprep_a3e_l0
	s_ashr_i32 s0, s11, 1
	v_sub_u32_e32 v6, s0, v32
	v_lshl_or_b32 v6, v6, 8, v3
	v_add_u32_e32 v7, -1, v42
	v_min_i32_e32 v6, v6, v7
	v_ashrrev_i32_e32 v7, 31, v6
	v_min_u32_e32 v8, 0xff, v22
	v_lshlrev_b32_e32 v8, 18, v8
	v_lshl_add_u64 v[6:7], v[6:7], 3, s[8:9]
	v_lshl_add_u64 v[6:7], v[6:7], 0, v[8:9]
	global_load_dword v52, v[6:7], off
	s_add_i32 s11, s11, s16
	s_cmp_le_u32 s10, 3
	s_cbranch_scc1 .Lprep_a3e_l0
	s_ashr_i32 s0, s11, 1
	v_sub_u32_e32 v6, s0, v33
	v_lshl_or_b32 v6, v6, 8, v3
	v_add_u32_e32 v7, -1, v43
	v_min_i32_e32 v6, v6, v7
	v_ashrrev_i32_e32 v7, 31, v6
	v_min_u32_e32 v8, 0xff, v23
	v_lshlrev_b32_e32 v8, 18, v8
	v_lshl_add_u64 v[6:7], v[6:7], 3, s[8:9]
	v_lshl_add_u64 v[6:7], v[6:7], 0, v[8:9]
	global_load_dword v53, v[6:7], off
	s_add_i32 s11, s11, s16
	s_cmp_le_u32 s10, 4
	s_cbranch_scc1 .Lprep_a3e_l0
	s_ashr_i32 s0, s11, 1
	v_sub_u32_e32 v6, s0, v34
	v_lshl_or_b32 v6, v6, 8, v3
	v_add_u32_e32 v7, -1, v44
	v_min_i32_e32 v6, v6, v7
	v_ashrrev_i32_e32 v7, 31, v6
	v_min_u32_e32 v8, 0xff, v24
	v_lshlrev_b32_e32 v8, 18, v8
	v_lshl_add_u64 v[6:7], v[6:7], 3, s[8:9]
	v_lshl_add_u64 v[6:7], v[6:7], 0, v[8:9]
	global_load_dword v54, v[6:7], off
	s_add_i32 s11, s11, s16
	s_cmp_le_u32 s10, 5
	s_cbranch_scc1 .Lprep_a3e_l0
	s_ashr_i32 s0, s11, 1
	v_sub_u32_e32 v6, s0, v35
	v_lshl_or_b32 v6, v6, 8, v3
	v_add_u32_e32 v7, -1, v45
	v_min_i32_e32 v6, v6, v7
	v_ashrrev_i32_e32 v7, 31, v6
	v_min_u32_e32 v8, 0xff, v25
	v_lshlrev_b32_e32 v8, 18, v8
	v_lshl_add_u64 v[6:7], v[6:7], 3, s[8:9]
	v_lshl_add_u64 v[6:7], v[6:7], 0, v[8:9]
	global_load_dword v55, v[6:7], off
	s_add_i32 s11, s11, s16
	s_cmp_le_u32 s10, 6
	s_cbranch_scc1 .Lprep_a3e_l0
	s_ashr_i32 s0, s11, 1
	v_sub_u32_e32 v6, s0, v36
	v_lshl_or_b32 v6, v6, 8, v3
	v_add_u32_e32 v7, -1, v46
	v_min_i32_e32 v6, v6, v7
	v_ashrrev_i32_e32 v7, 31, v6
	v_min_u32_e32 v8, 0xff, v26
	v_lshlrev_b32_e32 v8, 18, v8
	v_lshl_add_u64 v[6:7], v[6:7], 3, s[8:9]
	v_lshl_add_u64 v[6:7], v[6:7], 0, v[8:9]
	global_load_dword v56, v[6:7], off
	s_add_i32 s11, s11, s16
	s_cmp_le_u32 s10, 7
	s_cbranch_scc1 .Lprep_a3e_l0
	s_ashr_i32 s0, s11, 1
	v_sub_u32_e32 v6, s0, v37
	v_lshl_or_b32 v6, v6, 8, v3
	v_add_u32_e32 v7, -1, v47
	v_min_i32_e32 v6, v6, v7
	v_ashrrev_i32_e32 v7, 31, v6
	v_min_u32_e32 v8, 0xff, v27
	v_lshlrev_b32_e32 v8, 18, v8
	v_lshl_add_u64 v[6:7], v[6:7], 3, s[8:9]
	v_lshl_add_u64 v[6:7], v[6:7], 0, v[8:9]
	global_load_dword v57, v[6:7], off
	s_add_i32 s11, s11, s16
	s_cmp_le_u32 s10, 8
	s_cbranch_scc1 .Lprep_a3e_l0
	s_ashr_i32 s0, s11, 1
	v_sub_u32_e32 v6, s0, v38
	v_lshl_or_b32 v6, v6, 8, v3
	v_add_u32_e32 v7, -1, v48
	v_min_i32_e32 v6, v6, v7
	v_ashrrev_i32_e32 v7, 31, v6
	v_min_u32_e32 v8, 0xff, v28
	v_lshlrev_b32_e32 v8, 18, v8
	v_lshl_add_u64 v[6:7], v[6:7], 3, s[8:9]
	v_lshl_add_u64 v[6:7], v[6:7], 0, v[8:9]
	global_load_dword v58, v[6:7], off
	s_add_i32 s11, s11, s16
	s_cmp_le_u32 s10, 9
	s_cbranch_scc1 .Lprep_a3e_l0
	s_ashr_i32 s0, s11, 1
	v_sub_u32_e32 v6, s0, v39
	v_lshl_or_b32 v6, v6, 8, v3
	v_add_u32_e32 v7, -1, v49
	v_min_i32_e32 v6, v6, v7
	v_ashrrev_i32_e32 v7, 31, v6
	v_min_u32_e32 v8, 0xff, v29
	v_lshlrev_b32_e32 v8, 18, v8
	v_lshl_add_u64 v[6:7], v[6:7], 3, s[8:9]
	v_lshl_add_u64 v[6:7], v[6:7], 0, v[8:9]
	global_load_dword v59, v[6:7], off
	s_add_i32 s11, s11, s16
; #define LAS __attribute__((address_space(3)))
;     __device__ __forceinline__ bool next(int i, pg8::Unit& u) const { const int L = i * G + c; if (L >= 256) return false; u.pm = L >> 1; u.pn = L & 1; u.ord = i; return true; }
;     __device__ __forceinline__ int vcu() const { return (G % 8 == 0) ? (c % 8) * (G / 8) + c / 8 : c; }
;     __device__ __forceinline__ int vcu() const { return (G % 8 == 0) ? (c % 8) * (G / 8) + c / 8 : c; }
;     __device__ __forceinline__ bool next(int i, pg8::Unit& u) const { const int L = i * G + c; if (L >= 64) return false; u.pm = L >> 1; u.pn = L & 1; u.ord = i; return true; }
;     __device__ __forceinline__ bool next(int i, pg8::Unit& u) const {
;         const int L = i * G + vcu(); if (L >= nunits || i >= MOE_MAX_ORD) return false;
;         const int q = L >> 1; const int e = __builtin_amdgcn_readfirstlane((q < R) ? (int)((LAS unsigned short*)(lds + MOE_TAB_OFF + 2176))[q] : 256);
;     __device__ __forceinline__ void prepare() const {
;     ...
;                 token = list[(size_t)e * LISTCAP + lr].x / 10; }
;             else token = (u.pm - R) * 256 + r;
;             ((LAS unsigned short*)(lds + MOE_TOK_OFF))[i * 256 + r] = (unsigned short)token;
;         }
;         __syncthreads();
.Lprep_a3e_l0:
	s_waitcnt vmcnt(0)
	s_mov_b32 s11, s18
	s_cmp_le_u32 s10, 0
	s_cbranch_scc1 .Lprep_be_l0
	s_ashr_i32 s0, s11, 1
	s_sub_i32 s1, s0, s15
	v_mul_hi_i32 v6, v50, s17
	v_lshrrev_b32_e32 v7, 31, v6
	v_ashrrev_i32_e32 v6, 2, v6
	v_add_u32_e32 v6, v6, v7
	v_mov_b32_e32 v7, s1
	v_lshl_or_b32 v7, v7, 8, v3
	v_cmp_lt_u32_e32 vcc, 0xff, v20
	s_nop 1
	v_cndmask_b32_e32 v6, v6, v7, vcc
	ds_write_b16 v5, v6
	s_add_i32 s11, s11, s16
	s_cmp_le_u32 s10, 1
	s_cbranch_scc1 .Lprep_be_l0
	s_ashr_i32 s0, s11, 1
	s_sub_i32 s1, s0, s15
	v_mul_hi_i32 v6, v51, s17
	v_lshrrev_b32_e32 v7, 31, v6
	v_ashrrev_i32_e32 v6, 2, v6
	v_add_u32_e32 v6, v6, v7
	v_mov_b32_e32 v7, s1
	v_lshl_or_b32 v7, v7, 8, v3
	v_cmp_lt_u32_e32 vcc, 0xff, v21
	s_nop 1
	v_cndmask_b32_e32 v6, v6, v7, vcc
	ds_write_b16 v5, v6 offset:1024
	s_add_i32 s11, s11, s16
	s_cmp_le_u32 s10, 2
	s_cbranch_scc1 .Lprep_be_l0
	s_ashr_i32 s0, s11, 1
	s_sub_i32 s1, s0, s15
	v_mul_hi_i32 v6, v52, s17
	v_lshrrev_b32_e32 v7, 31, v6
	v_ashrrev_i32_e32 v6, 2, v6
	v_add_u32_e32 v6, v6, v7
	v_mov_b32_e32 v7, s1
	v_lshl_or_b32 v7, v7, 8, v3
	v_cmp_lt_u32_e32 vcc, 0xff, v22
	s_nop 1
	v_cndmask_b32_e32 v6, v6, v7, vcc
	ds_write_b16 v5, v6 offset:2048
	s_add_i32 s11, s11, s16
	s_cmp_le_u32 s10, 3
	s_cbranch_scc1 .Lprep_be_l0
	s_ashr_i32 s0, s11, 1
	s_sub_i32 s1, s0, s15
	v_mul_hi_i32 v6, v53, s17
	v_lshrrev_b32_e32 v7, 31, v6
	v_ashrrev_i32_e32 v6, 2, v6
	v_add_u32_e32 v6, v6, v7
	v_mov_b32_e32 v7, s1
	v_lshl_or_b32 v7, v7, 8, v3
	v_cmp_lt_u32_e32 vcc, 0xff, v23
	s_nop 1
	v_cndmask_b32_e32 v6, v6, v7, vcc
	ds_write_b16 v5, v6 offset:3072
	s_add_i32 s11, s11, s16
	s_cmp_le_u32 s10, 4
	s_cbranch_scc1 .Lprep_be_l0
	s_ashr_i32 s0, s11, 1
	s_sub_i32 s1, s0, s15
	v_mul_hi_i32 v6, v54, s17
	v_lshrrev_b32_e32 v7, 31, v6
	v_ashrrev_i32_e32 v6, 2, v6
	v_add_u32_e32 v6, v6, v7
	v_mov_b32_e32 v7, s1
	v_lshl_or_b32 v7, v7, 8, v3
	v_cmp_lt_u32_e32 vcc, 0xff, v24
	s_nop 1
	v_cndmask_b32_e32 v6, v6, v7, vcc
	ds_write_b16 v5, v6 offset:4096
	s_add_i32 s11, s11, s16
	s_cmp_le_u32 s10, 5
	s_cbranch_scc1 .Lprep_be_l0
	s_ashr_i32 s0, s11, 1
	s_sub_i32 s1, s0, s15
	v_mul_hi_i32 v6, v55, s17
	v_lshrrev_b32_e32 v7, 31, v6
	v_ashrrev_i32_e32 v6, 2, v6
	v_add_u32_e32 v6, v6, v7
	v_mov_b32_e32 v7, s1
	v_lshl_or_b32 v7, v7, 8, v3
	v_cmp_lt_u32_e32 vcc, 0xff, v25
	s_nop 1
	v_cndmask_b32_e32 v6, v6, v7, vcc
	ds_write_b16 v5, v6 offset:5120
	s_add_i32 s11, s11, s16
	s_cmp_le_u32 s10, 6
	s_cbranch_scc1 .Lprep_be_l0
	s_ashr_i32 s0, s11, 1
	s_sub_i32 s1, s0, s15
	v_mul_hi_i32 v6, v56, s17
	v_lshrrev_b32_e32 v7, 31, v6
	v_ashrrev_i32_e32 v6, 2, v6
	v_add_u32_e32 v6, v6, v7
	v_mov_b32_e32 v7, s1
	v_lshl_or_b32 v7, v7, 8, v3
	v_cmp_lt_u32_e32 vcc, 0xff, v26
	s_nop 1
	v_cndmask_b32_e32 v6, v6, v7, vcc
	ds_write_b16 v5, v6 offset:6144
	s_add_i32 s11, s11, s16
	s_cmp_le_u32 s10, 7
	s_cbranch_scc1 .Lprep_be_l0
	s_ashr_i32 s0, s11, 1
	s_sub_i32 s1, s0, s15
	v_mul_hi_i32 v6, v57, s17
	v_lshrrev_b32_e32 v7, 31, v6
	v_ashrrev_i32_e32 v6, 2, v6
	v_add_u32_e32 v6, v6, v7
	v_mov_b32_e32 v7, s1
	v_lshl_or_b32 v7, v7, 8, v3
	v_cmp_lt_u32_e32 vcc, 0xff, v27
	s_nop 1
	v_cndmask_b32_e32 v6, v6, v7, vcc
	ds_write_b16 v5, v6 offset:7168
	s_add_i32 s11, s11, s16
	s_cmp_le_u32 s10, 8
	s_cbranch_scc1 .Lprep_be_l0
	s_ashr_i32 s0, s11, 1
	s_sub_i32 s1, s0, s15
	v_mul_hi_i32 v6, v58, s17
	v_lshrrev_b32_e32 v7, 31, v6
	v_ashrrev_i32_e32 v6, 2, v6
	v_add_u32_e32 v6, v6, v7
	v_mov_b32_e32 v7, s1
	v_lshl_or_b32 v7, v7, 8, v3
	v_cmp_lt_u32_e32 vcc, 0xff, v28
	s_nop 1
	v_cndmask_b32_e32 v6, v6, v7, vcc
	ds_write_b16 v5, v6 offset:8192
	s_add_i32 s11, s11, s16
	s_cmp_le_u32 s10, 9
	s_cbranch_scc1 .Lprep_be_l0
	s_ashr_i32 s0, s11, 1
	s_sub_i32 s1, s0, s15
	v_mul_hi_i32 v6, v59, s17
	v_lshrrev_b32_e32 v7, 31, v6
	v_ashrrev_i32_e32 v6, 2, v6
	v_add_u32_e32 v6, v6, v7
	v_mov_b32_e32 v7, s1
	v_lshl_or_b32 v7, v7, 8, v3
	v_cmp_lt_u32_e32 vcc, 0xff, v29
	s_nop 1
	v_cndmask_b32_e32 v6, v6, v7, vcc
	ds_write_b16 v5, v6 offset:9216
	s_add_i32 s11, s11, s16
.Lprep_be_l0:
.LBB0_736:
	s_or_b64 exec, exec, s[6:7]
	s_cmp_ge_i32 s29, s28
	v_readfirstlane_b32 s10, v0
	s_waitcnt lgkmcnt(0)
	s_barrier
	s_cbranch_scc1 .LBB0_764
	s_ashr_i32 s54, s29, 1
	s_cmp_ge_i32 s54, s15
	v_mov_b32_e32 v3, 0x100
	s_cbranch_scc1 .LBB0_739
	s_lshl_b32 s0, s54, 1
	s_add_i32 s0, s0, 0
	s_add_i32 s0, s0, 0x20880
	v_mov_b32_e32 v1, s0
	ds_read_u16 v3, v1
